# gate/up epilogue top: redundant vmcnt(0) relaxed to vmcnt(16) (bias comes from LDS; next-unit prefetch loads may stay in flight through the epilogue)
# baseline (speedup 1.0000x reference)
.LBB0_252:
	s_nop 15
	s_nop 15
	v_ashrrev_i32_e32 v23, 31, v22
	s_ashr_i32 s67, s66, 31
	s_add_u32 s100, s50, s66
	s_addc_u32 s101, s51, s67
	s_add_u32 s100, s100, s52
	s_addc_u32 s101, s101, s53
	v_lshlrev_b64 v[250:251], 10, v[22:23]
	v_lshl_add_u64 v[250:251], v[250:251], 0, s[100:101]
	v_lshl_add_u64 v[250:251], v[250:251], 0, v[166:167]
	s_mov_b64 s[26:27], -1
	s_and_b64 vcc, exec, s[38:39]
	s_waitcnt vmcnt(16)
	s_waitcnt lgkmcnt(0)
	v_pk_fma_f32 v[26:27], v[154:155], s[24:25], v[2:3] op_sel_hi:[1,0,1]
	v_pk_fma_f32 v[18:19], v[160:161], s[24:25], v[12:13] op_sel_hi:[1,0,1]
	v_pk_fma_f32 v[20:21], v[158:159], s[24:25], v[10:11] op_sel_hi:[1,0,1]
	v_min_f32_e32 v18, 0x40e00000, v18
	v_min_f32_e32 v20, 0x40e00000, v20
	v_min_f32_e32 v21, 0x40e00000, v21
	v_pk_fma_f32 v[30:31], v[150:151], s[24:25], v[6:7] op_sel_hi:[1,0,1]
	v_min_f32_e32 v19, 0x40e00000, v19
	v_med3_f32 v30, v30, s19, v227
	v_med3_f32 v31, v31, s19, v227
	v_pk_add_f32 v[30:31], v[30:31], 1.0 op_sel_hi:[1,0]
	v_pk_fma_f32 v[32:33], v[148:149], s[24:25], v[16:17] op_sel_hi:[1,0,1]
	v_pk_mul_f32 v[148:149], v[20:21], s[28:29] op_sel_hi:[1,0]
	v_pk_mul_f32 v[20:21], v[20:21], v[30:31]
	v_pk_mul_f32 v[30:31], v[18:19], s[28:29] op_sel_hi:[1,0]
	v_pk_fma_f32 v[24:25], v[152:153], s[24:25], v[8:9] op_sel_hi:[1,0,1]
	v_exp_f32_e32 v30, v30
	v_exp_f32_e32 v31, v31
	v_med3_f32 v24, v24, s19, v227
	v_med3_f32 v25, v25, s19, v227
	v_pk_add_f32 v[24:25], v[24:25], 1.0 op_sel_hi:[1,0]
	v_pk_add_f32 v[30:31], v[30:31], 1.0 op_sel_hi:[1,0]
	v_pk_mul_f32 v[18:19], v[18:19], v[24:25]
	v_rcp_f32_e32 v30, v30
	v_rcp_f32_e32 v31, v31
	v_pk_fma_f32 v[146:147], v[146:147], s[24:25], v[14:15] op_sel_hi:[1,0,1]
	v_pk_fma_f32 v[28:29], v[156:157], s[24:25], v[4:5] op_sel_hi:[1,0,1]
	v_exp_f32_e32 v148, v148
	v_pk_mul_f32 v[24:25], v[18:19], v[30:31]
	v_min_f32_e32 v18, 0x40e00000, v26
	v_min_f32_e32 v19, 0x40e00000, v27
	v_pk_mul_f32 v[30:31], v[18:19], s[28:29] op_sel_hi:[1,0]
	v_med3_f32 v26, v146, s19, v227
	v_exp_f32_e32 v30, v30
	v_exp_f32_e32 v31, v31
	v_med3_f32 v27, v147, s19, v227
	v_pk_add_f32 v[26:27], v[26:27], 1.0 op_sel_hi:[1,0]
	v_exp_f32_e32 v149, v149
	v_pk_add_f32 v[30:31], v[30:31], 1.0 op_sel_hi:[1,0]
	v_pk_mul_f32 v[18:19], v[18:19], v[26:27]
	v_rcp_f32_e32 v30, v30
	v_rcp_f32_e32 v31, v31
	v_pk_add_f32 v[148:149], v[148:149], 1.0 op_sel_hi:[1,0]
	v_pk_fma_f32 v[134:135], v[134:135], s[24:25], v[6:7] op_sel_hi:[1,0,1]
	v_rcp_f32_e32 v148, v148
	v_pk_mul_f32 v[26:27], v[18:19], v[30:31]
	v_min_f32_e32 v18, 0x40e00000, v28
	v_min_f32_e32 v19, 0x40e00000, v29
	v_pk_mul_f32 v[30:31], v[18:19], s[28:29] op_sel_hi:[1,0]
	v_rcp_f32_e32 v149, v149
	v_exp_f32_e32 v30, v30
	v_exp_f32_e32 v31, v31
	v_med3_f32 v28, v32, s19, v227
	v_med3_f32 v29, v33, s19, v227
	v_pk_add_f32 v[28:29], v[28:29], 1.0 op_sel_hi:[1,0]
	v_pk_add_f32 v[30:31], v[30:31], 1.0 op_sel_hi:[1,0]
	v_pk_mul_f32 v[18:19], v[18:19], v[28:29]
	v_rcp_f32_e32 v30, v30
	v_rcp_f32_e32 v31, v31
	v_pk_mul_f32 v[20:21], v[20:21], v[148:149]
	v_pk_fma_f32 v[32:33], v[136:137], s[24:25], v[8:9] op_sel_hi:[1,0,1]
	v_pk_fma_f32 v[142:143], v[142:143], s[24:25], v[10:11] op_sel_hi:[1,0,1]
	v_pk_mul_f32 v[28:29], v[18:19], v[30:31]
	v_cvt_pk_fp8_f32 v19, v26, v27
	v_cvt_pk_fp8_f32 v18, v20, v21
	v_pk_fma_f32 v[30:31], v[144:145], s[24:25], v[12:13] op_sel_hi:[1,0,1]
	v_pk_fma_f32 v[20:21], v[140:141], s[24:25], v[4:5] op_sel_hi:[1,0,1]
	v_cvt_pk_fp8_f32 v19, v28, v29 op_sel:[0,0,1]
	v_pk_fma_f32 v[28:29], v[130:131], s[24:25], v[14:15] op_sel_hi:[1,0,1]
	v_cvt_pk_fp8_f32 v18, v24, v25 op_sel:[0,0,1]
	v_pk_fma_f32 v[26:27], v[138:139], s[24:25], v[2:3] op_sel_hi:[1,0,1]
	v_pk_fma_f32 v[24:25], v[132:133], s[24:25], v[16:17] op_sel_hi:[1,0,1]
	v_med3_f32 v132, v134, s19, v227
	v_med3_f32 v133, v135, s19, v227
	v_med3_f32 v32, v32, s19, v227
	v_med3_f32 v33, v33, s19, v227
	v_med3_f32 v28, v28, s19, v227
	v_med3_f32 v29, v29, s19, v227
	v_min_f32_e32 v130, 0x40e00000, v142
	v_min_f32_e32 v131, 0x40e00000, v143
	v_pk_add_f32 v[132:133], v[132:133], 1.0 op_sel_hi:[1,0]
	v_min_f32_e32 v30, 0x40e00000, v30
	v_min_f32_e32 v31, 0x40e00000, v31
	v_pk_add_f32 v[32:33], v[32:33], 1.0 op_sel_hi:[1,0]
	v_min_f32_e32 v26, 0x40e00000, v26
	v_min_f32_e32 v27, 0x40e00000, v27
	v_pk_add_f32 v[28:29], v[28:29], 1.0 op_sel_hi:[1,0]
	v_min_f32_e32 v20, 0x40e00000, v20
	v_min_f32_e32 v21, 0x40e00000, v21
	v_pk_mul_f32 v[134:135], v[130:131], s[28:29] op_sel_hi:[1,0]
	v_pk_mul_f32 v[130:131], v[130:131], v[132:133]
	v_pk_mul_f32 v[132:133], v[30:31], s[28:29] op_sel_hi:[1,0]
	v_pk_mul_f32 v[30:31], v[30:31], v[32:33]
	v_pk_mul_f32 v[32:33], v[26:27], s[28:29] op_sel_hi:[1,0]
	v_pk_mul_f32 v[26:27], v[26:27], v[28:29]
	v_pk_mul_f32 v[28:29], v[20:21], s[28:29] op_sel_hi:[1,0]
	v_exp_f32_e32 v134, v134
	v_exp_f32_e32 v135, v135
	v_exp_f32_e32 v32, v32
	v_exp_f32_e32 v33, v33
	v_exp_f32_e32 v28, v28
	v_exp_f32_e32 v29, v29
	v_pk_add_f32 v[134:135], v[134:135], 1.0 op_sel_hi:[1,0]
	v_exp_f32_e32 v132, v132
	v_exp_f32_e32 v133, v133
	v_pk_add_f32 v[32:33], v[32:33], 1.0 op_sel_hi:[1,0]
	v_pk_add_f32 v[28:29], v[28:29], 1.0 op_sel_hi:[1,0]
	v_rcp_f32_e32 v134, v134
	v_rcp_f32_e32 v135, v135
	v_rcp_f32_e32 v32, v32
	v_rcp_f32_e32 v33, v33
	v_rcp_f32_e32 v28, v28
	v_rcp_f32_e32 v29, v29
	v_med3_f32 v24, v24, s19, v227
	v_med3_f32 v25, v25, s19, v227
	v_pk_add_f32 v[24:25], v[24:25], 1.0 op_sel_hi:[1,0]
	v_pk_add_f32 v[132:133], v[132:133], 1.0 op_sel_hi:[1,0]
	v_pk_mul_f32 v[20:21], v[20:21], v[24:25]
	v_pk_mul_f32 v[130:131], v[130:131], v[134:135]
	v_rcp_f32_e32 v132, v132
	v_rcp_f32_e32 v133, v133
	v_pk_mul_f32 v[26:27], v[26:27], v[32:33]
	v_pk_mul_f32 v[24:25], v[20:21], v[28:29]
	v_cvt_pk_fp8_f32 v20, v130, v131
	v_cvt_pk_fp8_f32 v21, v26, v27
	v_pk_mul_f32 v[30:31], v[30:31], v[132:133]
	v_pk_fma_f32 v[32:33], v[116:117], s[24:25], v[16:17] op_sel_hi:[1,0,1]
	v_cvt_pk_fp8_f32 v20, v30, v31 op_sel:[0,0,1]
	v_cvt_pk_fp8_f32 v21, v24, v25 op_sel:[0,0,1]
	v_permlane16_swap_b32_e32 v18, v20
	v_permlane16_swap_b32_e32 v19, v21
	v_pk_fma_f32 v[30:31], v[118:119], s[24:25], v[6:7] op_sel_hi:[1,0,1]
	global_store_dwordx4 v[250:251], v[18:21], off
	v_med3_f32 v30, v30, s19, v227
	v_med3_f32 v31, v31, s19, v227
	v_pk_fma_f32 v[18:19], v[128:129], s[24:25], v[12:13] op_sel_hi:[1,0,1]
	v_pk_fma_f32 v[20:21], v[126:127], s[24:25], v[10:11] op_sel_hi:[1,0,1]
	v_pk_add_f32 v[30:31], v[30:31], 1.0 op_sel_hi:[1,0]
	v_min_f32_e32 v20, 0x40e00000, v20
	v_min_f32_e32 v21, 0x40e00000, v21
	v_min_f32_e32 v18, 0x40e00000, v18
	v_min_f32_e32 v19, 0x40e00000, v19
	v_pk_mul_f32 v[116:117], v[20:21], s[28:29] op_sel_hi:[1,0]
	v_pk_mul_f32 v[20:21], v[20:21], v[30:31]
	v_pk_mul_f32 v[30:31], v[18:19], s[28:29] op_sel_hi:[1,0]
	v_pk_fma_f32 v[28:29], v[120:121], s[24:25], v[8:9] op_sel_hi:[1,0,1]
	v_exp_f32_e32 v30, v30
	v_exp_f32_e32 v31, v31
	v_med3_f32 v28, v28, s19, v227
	v_med3_f32 v29, v29, s19, v227
	v_pk_add_f32 v[28:29], v[28:29], 1.0 op_sel_hi:[1,0]
	v_pk_add_f32 v[30:31], v[30:31], 1.0 op_sel_hi:[1,0]
	v_pk_fma_f32 v[26:27], v[122:123], s[24:25], v[2:3] op_sel_hi:[1,0,1]
	v_rcp_f32_e32 v30, v30
	v_rcp_f32_e32 v31, v31
	v_pk_mul_f32 v[18:19], v[18:19], v[28:29]
	v_pk_fma_f32 v[114:115], v[114:115], s[24:25], v[14:15] op_sel_hi:[1,0,1]
	v_pk_fma_f32 v[24:25], v[124:125], s[24:25], v[4:5] op_sel_hi:[1,0,1]
	v_pk_mul_f32 v[28:29], v[18:19], v[30:31]
	v_min_f32_e32 v18, 0x40e00000, v26
	v_min_f32_e32 v19, 0x40e00000, v27
	v_pk_mul_f32 v[30:31], v[18:19], s[28:29] op_sel_hi:[1,0]
	v_med3_f32 v26, v114, s19, v227
	v_exp_f32_e32 v30, v30
	v_exp_f32_e32 v31, v31
	v_med3_f32 v27, v115, s19, v227
	v_pk_add_f32 v[26:27], v[26:27], 1.0 op_sel_hi:[1,0]
	v_exp_f32_e32 v116, v116
	v_pk_add_f32 v[30:31], v[30:31], 1.0 op_sel_hi:[1,0]
	v_pk_mul_f32 v[18:19], v[18:19], v[26:27]
	v_rcp_f32_e32 v30, v30
	v_rcp_f32_e32 v31, v31
	v_exp_f32_e32 v117, v117
	v_pk_fma_f32 v[98:99], v[98:99], s[24:25], v[14:15] op_sel_hi:[1,0,1]
	v_pk_fma_f32 v[100:101], v[100:101], s[24:25], v[16:17] op_sel_hi:[1,0,1]
	v_pk_mul_f32 v[26:27], v[18:19], v[30:31]
	v_min_f32_e32 v18, 0x40e00000, v24
	v_min_f32_e32 v19, 0x40e00000, v25
	v_pk_mul_f32 v[30:31], v[18:19], s[28:29] op_sel_hi:[1,0]
	v_med3_f32 v24, v32, s19, v227
	v_exp_f32_e32 v30, v30
	v_exp_f32_e32 v31, v31
	v_med3_f32 v25, v33, s19, v227
	v_pk_add_f32 v[24:25], v[24:25], 1.0 op_sel_hi:[1,0]
	v_pk_add_f32 v[116:117], v[116:117], 1.0 op_sel_hi:[1,0]
	v_pk_add_f32 v[30:31], v[30:31], 1.0 op_sel_hi:[1,0]
	v_pk_mul_f32 v[18:19], v[18:19], v[24:25]
	v_rcp_f32_e32 v30, v30
	v_rcp_f32_e32 v31, v31
	v_rcp_f32_e32 v116, v116
	v_rcp_f32_e32 v117, v117
	v_pk_fma_f32 v[32:33], v[102:103], s[24:25], v[6:7] op_sel_hi:[1,0,1]
	v_pk_mul_f32 v[24:25], v[18:19], v[30:31]
	v_cvt_pk_fp8_f32 v19, v26, v27
	v_pk_mul_f32 v[20:21], v[20:21], v[116:117]
	v_cvt_pk_fp8_f32 v18, v20, v21
	v_cvt_pk_fp8_f32 v19, v24, v25 op_sel:[0,0,1]
	v_pk_fma_f32 v[20:21], v[112:113], s[24:25], v[12:13] op_sel_hi:[1,0,1]
	v_pk_fma_f32 v[24:25], v[110:111], s[24:25], v[10:11] op_sel_hi:[1,0,1]
	v_med3_f32 v32, v32, s19, v227
	v_med3_f32 v33, v33, s19, v227
	v_min_f32_e32 v24, 0x40e00000, v24
	v_min_f32_e32 v25, 0x40e00000, v25
	v_pk_add_f32 v[32:33], v[32:33], 1.0 op_sel_hi:[1,0]
	v_min_f32_e32 v20, 0x40e00000, v20
	v_min_f32_e32 v21, 0x40e00000, v21
	v_pk_mul_f32 v[102:103], v[24:25], s[28:29] op_sel_hi:[1,0]
	v_pk_mul_f32 v[24:25], v[24:25], v[32:33]
	v_pk_mul_f32 v[32:33], v[20:21], s[28:29] op_sel_hi:[1,0]
	v_pk_fma_f32 v[30:31], v[104:105], s[24:25], v[8:9] op_sel_hi:[1,0,1]
	v_exp_f32_e32 v32, v32
	v_exp_f32_e32 v33, v33
	v_med3_f32 v30, v30, s19, v227
	v_med3_f32 v31, v31, s19, v227
	v_pk_add_f32 v[30:31], v[30:31], 1.0 op_sel_hi:[1,0]
	v_pk_add_f32 v[32:33], v[32:33], 1.0 op_sel_hi:[1,0]
	v_cvt_pk_fp8_f32 v18, v28, v29 op_sel:[0,0,1]
	v_rcp_f32_e32 v32, v32
	v_rcp_f32_e32 v33, v33
	v_pk_fma_f32 v[28:29], v[106:107], s[24:25], v[2:3] op_sel_hi:[1,0,1]
	v_pk_mul_f32 v[20:21], v[20:21], v[30:31]
	v_pk_fma_f32 v[26:27], v[108:109], s[24:25], v[4:5] op_sel_hi:[1,0,1]
	v_pk_mul_f32 v[30:31], v[20:21], v[32:33]
	v_min_f32_e32 v20, 0x40e00000, v28
	v_min_f32_e32 v21, 0x40e00000, v29
	v_pk_mul_f32 v[32:33], v[20:21], s[28:29] op_sel_hi:[1,0]
	v_med3_f32 v28, v98, s19, v227
	v_exp_f32_e32 v32, v32
	v_exp_f32_e32 v33, v33
	v_med3_f32 v29, v99, s19, v227
	v_pk_add_f32 v[28:29], v[28:29], 1.0 op_sel_hi:[1,0]
	v_exp_f32_e32 v102, v102
	v_pk_add_f32 v[32:33], v[32:33], 1.0 op_sel_hi:[1,0]
	v_pk_mul_f32 v[20:21], v[20:21], v[28:29]
	v_rcp_f32_e32 v32, v32
	v_rcp_f32_e32 v33, v33
	v_exp_f32_e32 v103, v103
	v_pk_fma_f32 v[82:83], v[82:83], s[24:25], v[14:15] op_sel_hi:[1,0,1]
	v_pk_fma_f32 v[84:85], v[84:85], s[24:25], v[16:17] op_sel_hi:[1,0,1]
	v_pk_mul_f32 v[28:29], v[20:21], v[32:33]
	v_min_f32_e32 v20, 0x40e00000, v26
	v_min_f32_e32 v21, 0x40e00000, v27
	v_pk_mul_f32 v[32:33], v[20:21], s[28:29] op_sel_hi:[1,0]
	v_pk_add_f32 v[102:103], v[102:103], 1.0 op_sel_hi:[1,0]
	v_exp_f32_e32 v32, v32
	v_exp_f32_e32 v33, v33
	v_rcp_f32_e32 v102, v102
	v_rcp_f32_e32 v103, v103
	v_med3_f32 v26, v100, s19, v227
	v_pk_add_f32 v[32:33], v[32:33], 1.0 op_sel_hi:[1,0]
	v_med3_f32 v27, v101, s19, v227
	v_rcp_f32_e32 v32, v32
	v_rcp_f32_e32 v33, v33
	v_pk_add_f32 v[26:27], v[26:27], 1.0 op_sel_hi:[1,0]
	v_pk_mul_f32 v[24:25], v[24:25], v[102:103]
	v_pk_mul_f32 v[20:21], v[20:21], v[26:27]
	s_nop 0
	v_pk_mul_f32 v[26:27], v[20:21], v[32:33]
	v_cvt_pk_fp8_f32 v20, v24, v25
	v_cvt_pk_fp8_f32 v21, v28, v29
	v_cvt_pk_fp8_f32 v20, v30, v31 op_sel:[0,0,1]
	v_cvt_pk_fp8_f32 v21, v26, v27 op_sel:[0,0,1]
	v_permlane16_swap_b32_e32 v18, v20
	v_permlane16_swap_b32_e32 v19, v21
	s_mov_b64 s[100:101], 0x8000
	v_lshl_add_u64 v[24:25], v[250:251], 0, s[100:101]
	v_pk_fma_f32 v[32:33], v[86:87], s[24:25], v[6:7] op_sel_hi:[1,0,1]
	global_store_dwordx4 v[24:25], v[18:21], off
	v_med3_f32 v32, v32, s19, v227
	v_med3_f32 v33, v33, s19, v227
	v_pk_fma_f32 v[18:19], v[96:97], s[24:25], v[12:13] op_sel_hi:[1,0,1]
	v_pk_fma_f32 v[20:21], v[94:95], s[24:25], v[10:11] op_sel_hi:[1,0,1]
	v_pk_add_f32 v[32:33], v[32:33], 1.0 op_sel_hi:[1,0]
	v_min_f32_e32 v20, 0x40e00000, v20
	v_min_f32_e32 v21, 0x40e00000, v21
	v_min_f32_e32 v18, 0x40e00000, v18
	v_min_f32_e32 v19, 0x40e00000, v19
	v_pk_mul_f32 v[86:87], v[20:21], s[28:29] op_sel_hi:[1,0]
	v_pk_mul_f32 v[20:21], v[20:21], v[32:33]
	v_pk_mul_f32 v[32:33], v[18:19], s[28:29] op_sel_hi:[1,0]
	v_pk_fma_f32 v[30:31], v[88:89], s[24:25], v[8:9] op_sel_hi:[1,0,1]
	v_exp_f32_e32 v32, v32
	v_exp_f32_e32 v33, v33
	v_med3_f32 v30, v30, s19, v227
	v_med3_f32 v31, v31, s19, v227
	v_pk_add_f32 v[30:31], v[30:31], 1.0 op_sel_hi:[1,0]
	v_pk_add_f32 v[32:33], v[32:33], 1.0 op_sel_hi:[1,0]
	v_pk_fma_f32 v[28:29], v[90:91], s[24:25], v[2:3] op_sel_hi:[1,0,1]
	v_rcp_f32_e32 v32, v32
	v_rcp_f32_e32 v33, v33
	v_pk_mul_f32 v[18:19], v[18:19], v[30:31]
	v_pk_fma_f32 v[26:27], v[92:93], s[24:25], v[4:5] op_sel_hi:[1,0,1]
	v_exp_f32_e32 v86, v86
	v_pk_mul_f32 v[30:31], v[18:19], v[32:33]
	v_min_f32_e32 v18, 0x40e00000, v28
	v_min_f32_e32 v19, 0x40e00000, v29
	v_pk_mul_f32 v[32:33], v[18:19], s[28:29] op_sel_hi:[1,0]
	v_med3_f32 v28, v82, s19, v227
	v_exp_f32_e32 v32, v32
	v_exp_f32_e32 v33, v33
	v_med3_f32 v29, v83, s19, v227
	v_pk_add_f32 v[28:29], v[28:29], 1.0 op_sel_hi:[1,0]
	v_exp_f32_e32 v87, v87
	v_pk_add_f32 v[32:33], v[32:33], 1.0 op_sel_hi:[1,0]
	v_pk_mul_f32 v[18:19], v[18:19], v[28:29]
	v_rcp_f32_e32 v32, v32
	v_rcp_f32_e32 v33, v33
	v_pk_add_f32 v[86:87], v[86:87], 1.0 op_sel_hi:[1,0]
	v_rcp_f32_e32 v86, v86
	v_pk_mul_f32 v[28:29], v[18:19], v[32:33]
	v_min_f32_e32 v18, 0x40e00000, v26
	v_min_f32_e32 v19, 0x40e00000, v27
	v_pk_mul_f32 v[32:33], v[18:19], s[28:29] op_sel_hi:[1,0]
	v_rcp_f32_e32 v87, v87
	v_exp_f32_e32 v32, v32
	v_exp_f32_e32 v33, v33
	v_med3_f32 v26, v84, s19, v227
	v_med3_f32 v27, v85, s19, v227
	v_pk_add_f32 v[26:27], v[26:27], 1.0 op_sel_hi:[1,0]
	v_pk_add_f32 v[32:33], v[32:33], 1.0 op_sel_hi:[1,0]
	v_pk_mul_f32 v[18:19], v[18:19], v[26:27]
	v_rcp_f32_e32 v32, v32
	v_rcp_f32_e32 v33, v33
	v_pk_mul_f32 v[20:21], v[20:21], v[86:87]
	v_pk_mul_f32 v[26:27], v[18:19], v[32:33]
	v_cvt_pk_fp8_f32 v18, v20, v21
	v_cvt_pk_fp8_f32 v19, v28, v29
	v_pk_fma_f32 v[20:21], v[72:73], s[24:25], v[12:13] op_sel_hi:[1,0,1]
	v_cvt_pk_fp8_f32 v18, v30, v31 op_sel:[0,0,1]
	v_pk_fma_f32 v[30:31], v[66:67], s[24:25], v[2:3] op_sel_hi:[1,0,1]
	v_pk_fma_f32 v[66:67], v[78:79], s[24:25], v[6:7] op_sel_hi:[1,0,1]
	v_cvt_pk_fp8_f32 v19, v26, v27 op_sel:[0,0,1]
	v_pk_fma_f32 v[26:27], v[70:71], s[24:25], v[10:11] op_sel_hi:[1,0,1]
	v_med3_f32 v66, v66, s19, v227
	v_med3_f32 v67, v67, s19, v227
	v_min_f32_e32 v26, 0x40e00000, v26
	v_min_f32_e32 v27, 0x40e00000, v27
	v_pk_add_f32 v[66:67], v[66:67], 1.0 op_sel_hi:[1,0]
	v_min_f32_e32 v20, 0x40e00000, v20
	v_min_f32_e32 v21, 0x40e00000, v21
	v_pk_mul_f32 v[72:73], v[26:27], s[28:29] op_sel_hi:[1,0]
	v_pk_mul_f32 v[26:27], v[26:27], v[66:67]
	v_pk_mul_f32 v[66:67], v[20:21], s[28:29] op_sel_hi:[1,0]
	v_pk_fma_f32 v[32:33], v[80:81], s[24:25], v[8:9] op_sel_hi:[1,0,1]
	v_exp_f32_e32 v66, v66
	v_exp_f32_e32 v67, v67
	v_med3_f32 v32, v32, s19, v227
	v_med3_f32 v33, v33, s19, v227
	v_pk_add_f32 v[32:33], v[32:33], 1.0 op_sel_hi:[1,0]
	v_pk_add_f32 v[66:67], v[66:67], 1.0 op_sel_hi:[1,0]
	v_pk_mul_f32 v[20:21], v[20:21], v[32:33]
	v_rcp_f32_e32 v66, v66
	v_rcp_f32_e32 v67, v67
	v_pk_fma_f32 v[70:71], v[74:75], s[24:25], v[14:15] op_sel_hi:[1,0,1]
	v_pk_fma_f32 v[28:29], v[68:69], s[24:25], v[4:5] op_sel_hi:[1,0,1]
	v_exp_f32_e32 v72, v72
	v_pk_mul_f32 v[32:33], v[20:21], v[66:67]
	v_min_f32_e32 v20, 0x40e00000, v30
	v_min_f32_e32 v21, 0x40e00000, v31
	v_pk_mul_f32 v[66:67], v[20:21], s[28:29] op_sel_hi:[1,0]
	v_med3_f32 v30, v70, s19, v227
	v_exp_f32_e32 v66, v66
	v_exp_f32_e32 v67, v67
	v_med3_f32 v31, v71, s19, v227
	v_pk_add_f32 v[30:31], v[30:31], 1.0 op_sel_hi:[1,0]
	v_exp_f32_e32 v73, v73
	v_pk_add_f32 v[66:67], v[66:67], 1.0 op_sel_hi:[1,0]
	v_pk_mul_f32 v[20:21], v[20:21], v[30:31]
	v_rcp_f32_e32 v66, v66
	v_rcp_f32_e32 v67, v67
	v_pk_add_f32 v[72:73], v[72:73], 1.0 op_sel_hi:[1,0]
	v_pk_fma_f32 v[68:69], v[76:77], s[24:25], v[16:17] op_sel_hi:[1,0,1]
	v_rcp_f32_e32 v72, v72
	v_pk_mul_f32 v[30:31], v[20:21], v[66:67]
	v_min_f32_e32 v20, 0x40e00000, v28
	v_min_f32_e32 v21, 0x40e00000, v29
	v_pk_mul_f32 v[66:67], v[20:21], s[28:29] op_sel_hi:[1,0]
	v_rcp_f32_e32 v73, v73
	v_exp_f32_e32 v66, v66
	v_exp_f32_e32 v67, v67
	v_med3_f32 v28, v68, s19, v227
	v_med3_f32 v29, v69, s19, v227
	v_pk_add_f32 v[28:29], v[28:29], 1.0 op_sel_hi:[1,0]
	v_pk_add_f32 v[66:67], v[66:67], 1.0 op_sel_hi:[1,0]
	v_pk_mul_f32 v[20:21], v[20:21], v[28:29]
	v_rcp_f32_e32 v66, v66
	v_rcp_f32_e32 v67, v67
	v_pk_mul_f32 v[26:27], v[26:27], v[72:73]
	v_pk_mul_f32 v[28:29], v[20:21], v[66:67]
	v_cvt_pk_fp8_f32 v20, v26, v27
	v_cvt_pk_fp8_f32 v21, v30, v31
	s_mov_b64 s[100:101], 0x20000
	v_lshl_add_u64 v[24:25], v[250:251], 0, s[100:101]
	v_cvt_pk_fp8_f32 v20, v32, v33 op_sel:[0,0,1]
	v_cvt_pk_fp8_f32 v21, v28, v29 op_sel:[0,0,1]
	v_pk_fma_f32 v[30:31], v[62:63], s[24:25], v[6:7] op_sel_hi:[1,0,1]
	v_pk_fma_f32 v[28:29], v[64:65], s[24:25], v[8:9] op_sel_hi:[1,0,1]
	v_permlane16_swap_b32_e32 v18, v20
	v_permlane16_swap_b32_e32 v19, v21
	global_store_dwordx4 v[24:25], v[18:21], off
	v_med3_f32 v30, v30, s19, v227
	v_med3_f32 v31, v31, s19, v227
	v_pk_fma_f32 v[18:19], v[56:57], s[24:25], v[12:13] op_sel_hi:[1,0,1]
	v_pk_fma_f32 v[20:21], v[54:55], s[24:25], v[10:11] op_sel_hi:[1,0,1]
	v_pk_add_f32 v[30:31], v[30:31], 1.0 op_sel_hi:[1,0]
	v_min_f32_e32 v20, 0x40e00000, v20
	v_min_f32_e32 v21, 0x40e00000, v21
	v_min_f32_e32 v18, 0x40e00000, v18
	v_min_f32_e32 v19, 0x40e00000, v19
	v_pk_fma_f32 v[24:25], v[52:53], s[24:25], v[4:5] op_sel_hi:[1,0,1]
	v_pk_mul_f32 v[52:53], v[20:21], s[28:29] op_sel_hi:[1,0]
	v_pk_mul_f32 v[20:21], v[20:21], v[30:31]
	v_pk_mul_f32 v[30:31], v[18:19], s[28:29] op_sel_hi:[1,0]
	v_med3_f32 v28, v28, s19, v227
	v_exp_f32_e32 v30, v30
	v_exp_f32_e32 v31, v31
	v_med3_f32 v29, v29, s19, v227
	v_pk_add_f32 v[28:29], v[28:29], 1.0 op_sel_hi:[1,0]
	v_pk_fma_f32 v[26:27], v[50:51], s[24:25], v[2:3] op_sel_hi:[1,0,1]
	v_pk_add_f32 v[30:31], v[30:31], 1.0 op_sel_hi:[1,0]
	v_pk_mul_f32 v[18:19], v[18:19], v[28:29]
	v_rcp_f32_e32 v30, v30
	v_rcp_f32_e32 v31, v31
	v_pk_fma_f32 v[50:51], v[58:59], s[24:25], v[14:15] op_sel_hi:[1,0,1]
	v_exp_f32_e32 v52, v52
	v_exp_f32_e32 v53, v53
	v_pk_mul_f32 v[28:29], v[18:19], v[30:31]
	v_min_f32_e32 v18, 0x40e00000, v26
	v_min_f32_e32 v19, 0x40e00000, v27
	v_pk_mul_f32 v[30:31], v[18:19], s[28:29] op_sel_hi:[1,0]
	v_med3_f32 v26, v50, s19, v227
	v_exp_f32_e32 v30, v30
	v_exp_f32_e32 v31, v31
	v_med3_f32 v27, v51, s19, v227
	v_pk_add_f32 v[26:27], v[26:27], 1.0 op_sel_hi:[1,0]
	v_pk_add_f32 v[52:53], v[52:53], 1.0 op_sel_hi:[1,0]
	v_pk_add_f32 v[30:31], v[30:31], 1.0 op_sel_hi:[1,0]
	v_pk_mul_f32 v[18:19], v[18:19], v[26:27]
	v_rcp_f32_e32 v30, v30
	v_rcp_f32_e32 v31, v31
	v_pk_fma_f32 v[32:33], v[60:61], s[24:25], v[16:17] op_sel_hi:[1,0,1]
	v_rcp_f32_e32 v52, v52
	v_rcp_f32_e32 v53, v53
	v_pk_mul_f32 v[26:27], v[18:19], v[30:31]
	v_min_f32_e32 v18, 0x40e00000, v24
	v_min_f32_e32 v19, 0x40e00000, v25
	v_pk_mul_f32 v[30:31], v[18:19], s[28:29] op_sel_hi:[1,0]
	v_med3_f32 v24, v32, s19, v227
	v_exp_f32_e32 v30, v30
	v_exp_f32_e32 v31, v31
	v_med3_f32 v25, v33, s19, v227
	v_pk_add_f32 v[24:25], v[24:25], 1.0 op_sel_hi:[1,0]
	v_pk_fma_f32 v[6:7], v[46:47], s[24:25], v[6:7] op_sel_hi:[1,0,1]
	v_pk_add_f32 v[30:31], v[30:31], 1.0 op_sel_hi:[1,0]
	v_pk_mul_f32 v[18:19], v[18:19], v[24:25]
	v_rcp_f32_e32 v30, v30
	v_rcp_f32_e32 v31, v31
	v_pk_fma_f32 v[10:11], v[38:39], s[24:25], v[10:11] op_sel_hi:[1,0,1]
	v_med3_f32 v6, v6, s19, v227
	v_med3_f32 v7, v7, s19, v227
	v_pk_mul_f32 v[20:21], v[20:21], v[52:53]
	v_pk_mul_f32 v[24:25], v[18:19], v[30:31]
	v_pk_fma_f32 v[12:13], v[40:41], s[24:25], v[12:13] op_sel_hi:[1,0,1]
	v_min_f32_e32 v10, 0x40e00000, v10
	v_min_f32_e32 v11, 0x40e00000, v11
	v_pk_add_f32 v[6:7], v[6:7], 1.0 op_sel_hi:[1,0]
	v_cvt_pk_fp8_f32 v18, v20, v21
	v_pk_mul_f32 v[20:21], v[10:11], s[28:29] op_sel_hi:[1,0]
	v_pk_mul_f32 v[6:7], v[10:11], v[6:7]
	v_min_f32_e32 v10, 0x40e00000, v12
	v_min_f32_e32 v11, 0x40e00000, v13
	v_pk_mul_f32 v[12:13], v[10:11], s[28:29] op_sel_hi:[1,0]
	v_pk_fma_f32 v[8:9], v[48:49], s[24:25], v[8:9] op_sel_hi:[1,0,1]
	v_exp_f32_e32 v12, v12
	v_exp_f32_e32 v13, v13
	v_med3_f32 v8, v8, s19, v227
	v_med3_f32 v9, v9, s19, v227
	v_pk_fma_f32 v[2:3], v[34:35], s[24:25], v[2:3] op_sel_hi:[1,0,1]
	v_pk_add_f32 v[12:13], v[12:13], 1.0 op_sel_hi:[1,0]
	v_pk_add_f32 v[8:9], v[8:9], 1.0 op_sel_hi:[1,0]
	v_rcp_f32_e32 v12, v12
	v_rcp_f32_e32 v13, v13
	v_pk_mul_f32 v[8:9], v[10:11], v[8:9]
	v_min_f32_e32 v2, 0x40e00000, v2
	v_min_f32_e32 v3, 0x40e00000, v3
	v_pk_mul_f32 v[8:9], v[8:9], v[12:13]
	v_pk_mul_f32 v[12:13], v[2:3], s[28:29] op_sel_hi:[1,0]
	v_pk_fma_f32 v[14:15], v[42:43], s[24:25], v[14:15] op_sel_hi:[1,0,1]
	v_exp_f32_e32 v12, v12
	v_exp_f32_e32 v13, v13
	v_exp_f32_e32 v20, v20
	v_exp_f32_e32 v21, v21
	v_med3_f32 v10, v14, s19, v227
	v_pk_add_f32 v[12:13], v[12:13], 1.0 op_sel_hi:[1,0]
	v_med3_f32 v11, v15, s19, v227
	v_rcp_f32_e32 v12, v12
	v_rcp_f32_e32 v13, v13
	v_pk_fma_f32 v[4:5], v[36:37], s[24:25], v[4:5] op_sel_hi:[1,0,1]
	v_pk_add_f32 v[10:11], v[10:11], 1.0 op_sel_hi:[1,0]
	v_min_f32_e32 v4, 0x40e00000, v4
	v_pk_mul_f32 v[2:3], v[2:3], v[10:11]
	v_min_f32_e32 v5, 0x40e00000, v5
	v_pk_mul_f32 v[2:3], v[2:3], v[12:13]
	v_pk_mul_f32 v[12:13], v[4:5], s[28:29] op_sel_hi:[1,0]
	v_pk_add_f32 v[20:21], v[20:21], 1.0 op_sel_hi:[1,0]
	v_exp_f32_e32 v12, v12
	v_exp_f32_e32 v13, v13
	v_rcp_f32_e32 v20, v20
	v_rcp_f32_e32 v21, v21
	v_pk_add_f32 v[12:13], v[12:13], 1.0 op_sel_hi:[1,0]
	v_pk_fma_f32 v[16:17], v[44:45], s[24:25], v[16:17] op_sel_hi:[1,0,1]
	v_pk_mul_f32 v[6:7], v[6:7], v[20:21]
	v_rcp_f32_e32 v12, v12
	v_rcp_f32_e32 v13, v13
	v_cvt_pk_fp8_f32 v19, v26, v27
	v_med3_f32 v10, v16, s19, v227
	v_med3_f32 v11, v17, s19, v227
	v_cvt_pk_fp8_f32 v20, v6, v7
	v_cvt_pk_fp8_f32 v21, v2, v3
	v_pk_add_f32 v[10:11], v[10:11], 1.0 op_sel_hi:[1,0]
	v_pk_mul_f32 v[4:5], v[4:5], v[10:11]
	v_pk_mul_f32 v[4:5], v[4:5], v[12:13]
	v_cvt_pk_fp8_f32 v18, v28, v29 op_sel:[0,0,1]
	v_cvt_pk_fp8_f32 v19, v24, v25 op_sel:[0,0,1]
	v_cvt_pk_fp8_f32 v20, v8, v9 op_sel:[0,0,1]
	v_cvt_pk_fp8_f32 v21, v4, v5 op_sel:[0,0,1]
	v_permlane16_swap_b32_e32 v18, v20
	v_permlane16_swap_b32_e32 v19, v21
	s_mov_b64 s[100:101], 0x28000
	v_lshl_add_u64 v[2:3], v[250:251], 0, s[100:101]
	global_store_dwordx4 v[2:3], v[18:21], off
	s_cbranch_vccnz .LBB0_237
	s_andn2_b64 vcc, exec, s[42:43]
	s_cbranch_vccnz .LBB0_236
	s_barrier
	s_branch .LBB0_236
